# baseline (speedup 1.0000x reference)
_Z12conv1_kernelPKfPKDF16_S0_PDF16_:
	s_endpgm
	s_endpgm
	s_endpgm
	s_endpgm
	s_endpgm
	s_endpgm
	s_endpgm
	s_endpgm
	s_endpgm
	s_endpgm
	s_endpgm
	s_endpgm
	s_endpgm
	s_endpgm
	s_endpgm
	s_endpgm
	s_endpgm
	s_endpgm
	s_endpgm
	s_endpgm
	s_endpgm
	s_endpgm
	s_endpgm
	s_endpgm
	s_endpgm
	s_endpgm
	s_endpgm
	s_endpgm
	s_endpgm
	s_endpgm
	s_endpgm
	s_endpgm
	s_endpgm
	s_endpgm
	s_endpgm
	s_endpgm
	s_endpgm
	s_endpgm
	s_endpgm
	s_endpgm
	s_endpgm
	s_endpgm
	s_endpgm
	s_endpgm
	s_endpgm
	s_endpgm
	s_endpgm
	s_endpgm
	s_endpgm
	s_endpgm
	s_endpgm
	s_endpgm
	s_endpgm
	s_endpgm
	s_endpgm
	s_endpgm
	s_endpgm
	s_endpgm
	s_endpgm
	s_endpgm
	s_endpgm
	s_endpgm
	s_endpgm
	s_endpgm
	s_endpgm
	s_endpgm
	s_endpgm
	s_endpgm
	s_endpgm
	s_endpgm
	s_endpgm
	s_endpgm
	s_endpgm
	s_endpgm
	s_endpgm
	s_endpgm
	s_endpgm
	s_endpgm
	s_endpgm
	s_endpgm
	s_endpgm
	s_endpgm
	s_endpgm
	s_endpgm
	s_endpgm
	s_endpgm
	s_endpgm
	s_endpgm
	s_endpgm
	s_endpgm
	s_endpgm
	s_endpgm
	s_endpgm
	s_endpgm
	s_endpgm
	s_endpgm
	s_endpgm
	s_endpgm
	s_endpgm
	s_endpgm
	s_endpgm
	s_endpgm
	s_endpgm
	s_endpgm
	s_endpgm
	s_endpgm
	s_endpgm
	s_endpgm
	s_endpgm
	s_endpgm
	s_endpgm
	s_endpgm
	s_endpgm
	s_endpgm
	s_endpgm
	s_endpgm
	s_endpgm
	s_endpgm
	s_endpgm
	s_endpgm
	s_endpgm
	s_endpgm
	s_endpgm
	s_endpgm
	s_endpgm
	s_endpgm
	s_endpgm
	s_endpgm
	s_endpgm
	s_endpgm
	s_endpgm
	s_endpgm
	s_endpgm
	s_endpgm
	s_endpgm
	s_endpgm
	s_endpgm
	s_endpgm
	s_endpgm
	s_endpgm
	s_endpgm
	s_endpgm
	s_endpgm
	s_endpgm
	s_endpgm
	s_endpgm
	s_endpgm
	s_endpgm
	s_endpgm
	s_endpgm
	s_endpgm
	s_endpgm
	s_endpgm
	s_endpgm
	s_endpgm
	s_endpgm
	s_endpgm
	s_endpgm
	s_endpgm
	s_endpgm
	s_endpgm
	s_endpgm
	s_endpgm
	s_endpgm
	s_endpgm
	s_endpgm
	s_endpgm
	s_endpgm
	s_endpgm
	s_endpgm
	s_endpgm
	s_endpgm
	s_endpgm
	s_endpgm
	s_endpgm
	s_endpgm
	s_endpgm
	s_endpgm
	s_endpgm
	s_endpgm
	s_endpgm
	s_endpgm
	s_endpgm
	s_endpgm
	s_endpgm
	s_endpgm
	s_endpgm
	s_endpgm
	s_endpgm
	s_endpgm
	s_endpgm
	s_endpgm
	s_endpgm

_Z11gat3_kernelPKfPKDF16_S0_Pf:
	s_endpgm

_Z12gat3p_kernelPKfPKDF16_S0_S0_S0_S0_Pf:
	s_endpgm

_Z12final_kernelPKfS0_S0_Pf:
	s_endpgm
	s_endpgm
	s_endpgm
	s_endpgm
	s_endpgm
	s_endpgm
	s_endpgm
	s_endpgm
	s_endpgm
	s_endpgm
	s_endpgm
	s_endpgm
	s_endpgm
	s_endpgm
	s_endpgm
	s_endpgm
	s_endpgm
	s_endpgm
	s_endpgm
	s_endpgm
	s_endpgm
	s_endpgm
	s_endpgm
	s_endpgm
	s_endpgm
	s_endpgm
	s_endpgm
	s_endpgm
	s_endpgm
	s_endpgm
	s_endpgm
	s_endpgm
	s_endpgm
	s_endpgm
	s_endpgm
	s_endpgm
	s_endpgm
	s_endpgm
	s_endpgm
	s_endpgm
	s_endpgm
	s_endpgm
	s_endpgm
	s_endpgm
	s_endpgm
	s_endpgm
	s_endpgm
	s_endpgm
	s_endpgm
